# attn_dsa PV: V^T fragment batches 1-3 read behind the previous batch's MFMAs, counted lgkmcnt waits, on top of v90
# baseline (speedup 1.0000x reference)
.LBB0_1324:
	v_sub_f32_e32 v70, v70, v203
	v_exp_f32_e32 v209, v70
	v_sub_f32_e32 v70, v87, v203
	v_exp_f32_e32 v210, v70
	v_sub_f32_e32 v70, v71, v203
	v_exp_f32_e32 v211, v70
	v_sub_f32_e32 v70, v88, v203
	v_sub_f32_e32 v84, v84, v203
	v_exp_f32_e32 v71, v70
	v_sub_f32_e32 v70, v72, v203
	v_sub_f32_e32 v72, v73, v203
	v_exp_f32_e32 v204, v84
	v_exp_f32_e32 v84, v72
	v_sub_f32_e32 v72, v90, v203
	v_sub_f32_e32 v69, v69, v203
	v_exp_f32_e32 v73, v72
	v_sub_f32_e32 v72, v74, v203
	v_sub_f32_e32 v74, v75, v203
	v_exp_f32_e32 v206, v69
	v_sub_f32_e32 v69, v86, v203
	v_exp_f32_e32 v86, v74
	v_sub_f32_e32 v74, v92, v203
	v_exp_f32_e32 v183, v74
	v_sub_f32_e32 v74, v76, v203
	v_exp_f32_e32 v185, v74
	v_sub_f32_e32 v74, v93, v203
	v_exp_f32_e32 v182, v74
	v_sub_f32_e32 v74, v77, v203
	v_exp_f32_e32 v184, v74
	v_sub_f32_e32 v74, v94, v203
	v_exp_f32_e32 v93, v74
	v_sub_f32_e32 v74, v78, v203
	v_exp_f32_e32 v187, v74
	v_sub_f32_e32 v74, v95, v203
	v_exp_f32_e32 v92, v74
	v_sub_f32_e32 v74, v79, v203
	v_exp_f32_e32 v186, v74
	v_sub_f32_e32 v74, v96, v203
	v_exp_f32_e32 v79, v74
	v_sub_f32_e32 v74, v80, v203
	v_exp_f32_e32 v95, v74
	v_sub_f32_e32 v74, v97, v203
	v_exp_f32_e32 v78, v74
	v_sub_f32_e32 v74, v81, v203
	v_exp_f32_e32 v94, v74
	v_sub_f32_e32 v74, v98, v203
	v_exp_f32_e32 v81, v74
	v_sub_f32_e32 v74, v82, v203
	v_sub_f32_e32 v68, v68, v203
	v_exp_f32_e32 v97, v74
	v_sub_f32_e32 v74, v99, v203
	v_exp_f32_e32 v205, v68
	v_sub_f32_e32 v68, v85, v203
	v_exp_f32_e32 v85, v70
	v_exp_f32_e32 v87, v72
	v_exp_f32_e32 v80, v74
	v_sub_f32_e32 v74, v83, v203
	v_exp_f32_e32 v96, v74
	v_sub_f32_e32 v70, v89, v203
	v_exp_f32_e32 v70, v70
	v_exp_f32_e32 v68, v68
	v_pk_mov_b32 v[74:75], v[84:85], v[84:85] op_sel:[1,0]
	v_pk_mov_b32 v[76:77], v[86:87], v[86:87] op_sel:[1,0]
	v_exp_f32_e32 v69, v69
	v_pk_add_f32 v[190:191], v[78:79], v[94:95]
	v_pk_add_f32 v[192:193], v[80:81], v[96:97]
	v_cvt_pk_bf16_f32 v74, v74, v75
	v_cvt_pk_bf16_f32 v75, v76, v77
	v_pk_mov_b32 v[76:77], v[182:183], v[182:183] op_sel:[1,0]
	v_pk_mov_b32 v[82:83], v[92:93], v[92:93] op_sel:[1,0]
	v_pk_mov_b32 v[78:79], v[78:79], v[78:79] op_sel:[1,0]
	v_pk_mov_b32 v[80:81], v[80:81], v[80:81] op_sel:[1,0]
	v_cvt_pk_bf16_f32 v76, v76, v77
	v_cvt_pk_bf16_f32 v77, v82, v83
	v_cvt_pk_bf16_f32 v78, v78, v79
	v_cvt_pk_bf16_f32 v79, v80, v81
	v_pk_mov_b32 v[80:81], v[184:185], v[184:185] op_sel:[1,0]
	v_pk_mov_b32 v[82:83], v[186:187], v[186:187] op_sel:[1,0]
	v_add_f32_e32 v207, v204, v205
	v_pk_add_f32 v[88:89], v[70:71], v[84:85]
	v_cvt_pk_bf16_f32 v80, v80, v81
	v_cvt_pk_bf16_f32 v81, v82, v83
	v_pk_mov_b32 v[82:83], v[94:95], v[94:95] op_sel:[1,0]
	v_pk_mov_b32 v[84:85], v[96:97], v[96:97] op_sel:[1,0]
	v_add_f32_e32 v208, v68, v206
	v_sub_f32_e32 v72, v91, v203
	v_cvt_pk_bf16_f32 v82, v82, v83
	v_cvt_pk_bf16_f32 v83, v84, v85
	v_add_f32_e32 v84, 0, v207
	v_exp_f32_e32 v72, v72
	v_add_f32_e32 v212, v69, v209
	v_add_f32_e32 v84, v208, v84
	v_add_f32_e32 v213, v210, v211
	v_add_f32_e32 v84, v212, v84
	v_add_f32_e32 v84, v213, v84
	v_add_f32_e32 v84, v89, v84
	v_pk_add_f32 v[90:91], v[72:73], v[86:87]
	v_add_f32_e32 v84, v88, v84
	v_add_f32_e32 v84, v91, v84
	v_pk_add_f32 v[98:99], v[182:183], v[184:185]
	v_add_f32_e32 v84, v90, v84
	v_add_f32_e32 v84, v99, v84
	v_pk_add_f32 v[188:189], v[92:93], v[186:187]
	v_add_f32_e32 v84, v98, v84
	v_add3_u32 v183, s24, v169, v1
	v_add_f32_e32 v84, v189, v84
	v_add_u32_e32 v96, 0x4000, v183
	v_add_f32_e32 v182, v188, v84
	ds_read2_b64 v[84:87], v96 offset0:128 offset1:130
	ds_read2_b64 v[88:91], v96 offset0:132 offset1:134
	ds_read2_b64 v[92:95], v96 offset0:136 offset1:138
	ds_read2_b64 v[96:99], v96 offset0:140 offset1:142
	v_add_f32_e32 v182, v191, v182
	v_add_f32_e32 v182, v190, v182
	v_pk_mov_b32 v[70:71], v[70:71], v[70:71] op_sel:[1,0]
	v_pk_mov_b32 v[72:73], v[72:73], v[72:73] op_sel:[1,0]
	v_add_f32_e32 v182, v193, v182
	v_cvt_pk_bf16_f32 v68, v204, v68
	v_cvt_pk_bf16_f32 v69, v69, v210
	v_cvt_pk_bf16_f32 v70, v70, v71
	v_cvt_pk_bf16_f32 v71, v72, v73
	v_cvt_pk_bf16_f32 v72, v205, v206
	v_cvt_pk_bf16_f32 v73, v209, v211
	v_add_f32_e32 v182, v192, v182
	s_waitcnt lgkmcnt(0)
	v_mfma_f32_32x32x16_bf16 v[52:67], v[84:87], v[68:71], v[52:67]
	v_add_u32_e32 v84, 0x5000, v183
	ds_read2_b64 v[84:87], v84 offset0:160 offset1:162
	v_mfma_f32_32x32x16_bf16 v[52:67], v[88:91], v[76:79], v[52:67]
	v_add_u32_e32 v88, 0x5000, v183
	ds_read2_b64 v[88:91], v88 offset0:164 offset1:166
	v_mfma_f32_32x32x16_bf16 v[52:67], v[92:95], v[72:75], v[52:67]
	v_add_u32_e32 v92, 0x5000, v183
	ds_read2_b64 v[92:95], v92 offset0:168 offset1:170
	v_mfma_f32_32x32x16_bf16 v[52:67], v[96:99], v[80:83], v[52:67]
	v_add_u32_e32 v96, 0x5000, v183
	ds_read2_b64 v[96:99], v96 offset0:172 offset1:174
	s_waitcnt lgkmcnt(3)
	v_mfma_f32_32x32x16_bf16 v[36:51], v[84:87], v[68:71], v[36:51]
	v_add_u32_e32 v84, 0x6000, v183
	ds_read2_b64 v[84:87], v84 offset0:192 offset1:194
	s_waitcnt lgkmcnt(3)
	v_mfma_f32_32x32x16_bf16 v[36:51], v[88:91], v[76:79], v[36:51]
	v_add_u32_e32 v88, 0x6000, v183
	ds_read2_b64 v[88:91], v88 offset0:196 offset1:198
	s_waitcnt lgkmcnt(3)
	v_mfma_f32_32x32x16_bf16 v[36:51], v[92:95], v[72:75], v[36:51]
	v_add_u32_e32 v92, 0x6000, v183
	ds_read2_b64 v[92:95], v92 offset0:200 offset1:202
	s_waitcnt lgkmcnt(3)
	v_mfma_f32_32x32x16_bf16 v[36:51], v[96:99], v[80:83], v[36:51]
	v_add_u32_e32 v96, 0x6000, v183
	ds_read2_b64 v[96:99], v96 offset0:204 offset1:206
	s_waitcnt lgkmcnt(3)
	v_mfma_f32_32x32x16_bf16 v[20:35], v[84:87], v[68:71], v[20:35]
	v_add_u32_e32 v84, 0x7000, v183
	ds_read2_b64 v[84:87], v84 offset0:224 offset1:226
	s_waitcnt lgkmcnt(3)
	v_mfma_f32_32x32x16_bf16 v[20:35], v[88:91], v[76:79], v[20:35]
	v_add_u32_e32 v88, 0x7000, v183
	ds_read2_b64 v[88:91], v88 offset0:228 offset1:230
	s_waitcnt lgkmcnt(3)
	v_mfma_f32_32x32x16_bf16 v[20:35], v[92:95], v[72:75], v[20:35]
	v_add_u32_e32 v92, 0x7000, v183
	ds_read2_b64 v[92:95], v92 offset0:232 offset1:234
	s_waitcnt lgkmcnt(3)
	v_mfma_f32_32x32x16_bf16 v[20:35], v[96:99], v[80:83], v[20:35]
	v_add_u32_e32 v96, 0x7000, v183
	ds_read2_b64 v[96:99], v96 offset0:236 offset1:238
	s_waitcnt lgkmcnt(3)
	v_mfma_f32_32x32x16_bf16 v[4:19], v[84:87], v[68:71], v[4:19]
	s_waitcnt lgkmcnt(2)
	v_mfma_f32_32x32x16_bf16 v[4:19], v[88:91], v[76:79], v[4:19]
	s_waitcnt lgkmcnt(1)
	v_mfma_f32_32x32x16_bf16 v[4:19], v[92:95], v[72:75], v[4:19]
	s_waitcnt lgkmcnt(0)
	v_mfma_f32_32x32x16_bf16 v[4:19], v[96:99], v[80:83], v[4:19]
	v_add_f32_e32 v151, v182, v151
	s_andn2_b64 vcc, exec, s[12:13]
	s_cbranch_vccz .LBB0_1221
	s_branch .LBB0_1222
